# packed f32 VOP3P ops in P7/P8 epilogues split into two single f32 ops (bit-identical)
# baseline (speedup 1.0000x reference)
.Lp7pub_skip:
	s_nop 15
	s_nop 15
	s_lshl_b32 s0, s96, 10
	s_and_b32 s0, s0, 0x400
	v_mbcnt_lo_u32_b32 v2, -1, 0
	v_mbcnt_hi_u32_b32 v2, -1, v2
	s_add_i32 s0, s0, 0
	v_ashrrev_i32_e32 v5, 4, v2
	v_lshl_add_u32 v134, v5, 3, s92
	v_lshl_add_u32 v135, v134, 2, s0
	s_lshr_b32 s0, s33, 1
	s_and_b32 s0, s0, 0x380
	v_add_u32_e32 v151, 0x21000, v135
	v_add_u32_e32 v164, s0, v134
	ds_read_b128 v[138:141], v151
	ds_read_b128 v[134:137], v151 offset:16
	ds_read_b128 v[142:145], v151 offset:512
	v_and_b32_e32 v5, 1, v5
	v_and_or_b32 v2, v2, 15, s89
	v_ashrrev_i32_e32 v165, 31, v164
	s_waitcnt lgkmcnt(0)
	v_add_f32_e32 v188, v126, v134
	v_add_f32_e32 v189, v127, v135
	v_add_f32_e32 v168, 1.0, v144
	v_add_f32_e32 v169, 1.0, v145
	v_add_f32_e32 v170, 1.0, v142
	v_add_f32_e32 v171, 1.0, v143
	ds_read_b128 v[142:145], v151 offset:528
	v_add_f32_e32 v192, v98, v170
	v_add_f32_e32 v193, v99, v171
	v_add_f32_e32 v190, v100, v168
	v_add_f32_e32 v191, v101, v169
	v_med3_f32 v192, v192, s9, v183
	s_waitcnt lgkmcnt(0)
	v_add_f32_e32 v174, 1.0, v142
	v_add_f32_e32 v175, 1.0, v143
	v_lshlrev_b32_e32 v142, 3, v5
	v_ashrrev_i32_e32 v143, 31, v142
	v_sub_co_u32_e32 v166, vcc, 0, v142
	v_add_f32_e32 v172, 1.0, v144
	v_add_f32_e32 v173, 1.0, v145
	s_nop 0
	v_subb_co_u32_e32 v167, vcc, 0, v143, vcc
	v_add_f32_e32 v142, v132, v140
	v_add_f32_e32 v143, v133, v141
	v_add_f32_e32 v144, v130, v138
	v_add_f32_e32 v145, v131, v139
	v_med3_f32 v193, v193, s9, v183
	v_min_f32_e32 v144, 0x40e00000, v144
	v_min_f32_e32 v145, 0x40e00000, v145
	v_min_f32_e32 v142, 0x40e00000, v142
	v_min_f32_e32 v143, 0x40e00000, v143
	v_mul_f32_e32 v198, s50, v144
	v_mul_f32_e32 v199, s50, v145
	v_mul_f32_e32 v144, v144, v192
	v_mul_f32_e32 v145, v145, v193
	v_mul_f32_e32 v192, s50, v142
	v_mul_f32_e32 v193, s50, v143
	v_med3_f32 v190, v190, s9, v183
	v_exp_f32_e32 v192, v192
	v_exp_f32_e32 v193, v193
	v_med3_f32 v191, v191, s9, v183
	v_mul_f32_e32 v142, v142, v190
	v_mul_f32_e32 v143, v143, v191
	v_add_f32_e32 v196, v94, v174
	v_add_f32_e32 v197, v95, v175
	v_add_f32_e32 v192, 1.0, v192
	v_add_f32_e32 v193, 1.0, v193
	v_add_f32_e32 v186, v128, v136
	v_add_f32_e32 v187, v129, v137
	v_rcp_f32_e32 v192, v192
	v_rcp_f32_e32 v193, v193
	v_exp_f32_e32 v198, v198
	v_exp_f32_e32 v199, v199
	v_add_f32_e32 v194, v96, v172
	v_add_f32_e32 v195, v97, v173
	v_mul_f32_e32 v190, v142, v192
	v_mul_f32_e32 v191, v143, v193
	v_min_f32_e32 v142, 0x40e00000, v188
	v_min_f32_e32 v143, 0x40e00000, v189
	v_mul_f32_e32 v188, s50, v142
	v_mul_f32_e32 v189, s50, v143
	v_med3_f32 v192, v196, s9, v183
	v_exp_f32_e32 v188, v188
	v_exp_f32_e32 v189, v189
	v_med3_f32 v193, v197, s9, v183
	v_mul_f32_e32 v142, v142, v192
	v_mul_f32_e32 v143, v143, v193
	v_med3_f32 v192, v194, s9, v183
	v_add_f32_e32 v188, 1.0, v188
	v_add_f32_e32 v189, 1.0, v189
	v_med3_f32 v193, v195, s9, v183
	v_rcp_f32_e32 v188, v188
	v_rcp_f32_e32 v189, v189
	v_add_f32_e32 v198, 1.0, v198
	v_add_f32_e32 v199, 1.0, v199
	v_add_f32_e32 v194, v90, v170
	v_add_f32_e32 v195, v91, v171
	v_rcp_f32_e32 v198, v198
	v_mul_f32_e32 v188, v142, v188
	v_mul_f32_e32 v189, v143, v189
	v_min_f32_e32 v142, 0x40e00000, v186
	v_min_f32_e32 v143, 0x40e00000, v187
	v_mul_f32_e32 v186, s50, v142
	v_mul_f32_e32 v187, s50, v143
	v_mul_f32_e32 v142, v142, v192
	v_mul_f32_e32 v143, v143, v193
	v_exp_f32_e32 v186, v186
	v_exp_f32_e32 v187, v187
	v_rcp_f32_e32 v199, v199
	v_med3_f32 v194, v194, s9, v183
	v_med3_f32 v195, v195, s9, v183
	v_add_f32_e32 v186, 1.0, v186
	v_add_f32_e32 v187, 1.0, v187
	v_mul_f32_e32 v144, v144, v198
	v_mul_f32_e32 v145, v145, v199
	v_rcp_f32_e32 v186, v186
	v_rcp_f32_e32 v187, v187
	v_add_f32_e32 v192, v92, v168
	v_add_f32_e32 v193, v93, v169
	v_add_f32_e32 v198, v86, v174
	v_add_f32_e32 v199, v87, v175
	v_med3_f32 v192, v192, s9, v183
	v_mul_f32_e32 v186, v142, v186
	v_mul_f32_e32 v187, v143, v187
	v_mov_b32_e32 v143, v3
	v_cvt_pk_fp8_f32 v143, v188, v189
	v_mov_b32_e32 v142, v3
	v_cvt_pk_fp8_f32 v142, v144, v145
	v_add_f32_e32 v144, v124, v140
	v_add_f32_e32 v145, v125, v141
	v_cvt_pk_fp8_f32 v143, v186, v187 op_sel:[0,0,1]
	v_add_f32_e32 v186, v122, v138
	v_add_f32_e32 v187, v123, v139
	v_min_f32_e32 v144, 0x40e00000, v144
	v_min_f32_e32 v186, 0x40e00000, v186
	v_min_f32_e32 v187, 0x40e00000, v187
	v_min_f32_e32 v145, 0x40e00000, v145
	v_mul_f32_e32 v200, s50, v186
	v_mul_f32_e32 v201, s50, v187
	v_mul_f32_e32 v186, v186, v194
	v_mul_f32_e32 v187, v187, v195
	v_mul_f32_e32 v194, s50, v144
	v_mul_f32_e32 v195, s50, v145
	v_med3_f32 v193, v193, s9, v183
	v_exp_f32_e32 v194, v194
	v_exp_f32_e32 v195, v195
	v_cvt_pk_fp8_f32 v142, v190, v191 op_sel:[0,0,1]
	v_add_f32_e32 v190, v118, v134
	v_add_f32_e32 v191, v119, v135
	v_mul_f32_e32 v144, v144, v192
	v_mul_f32_e32 v145, v145, v193
	v_add_f32_e32 v194, 1.0, v194
	v_add_f32_e32 v195, 1.0, v195
	v_add_f32_e32 v188, v120, v136
	v_add_f32_e32 v189, v121, v137
	v_rcp_f32_e32 v194, v194
	v_rcp_f32_e32 v195, v195
	v_exp_f32_e32 v200, v200
	v_exp_f32_e32 v201, v201
	v_add_f32_e32 v196, v88, v172
	v_add_f32_e32 v197, v89, v173
	v_mul_f32_e32 v192, v144, v194
	v_mul_f32_e32 v193, v145, v195
	v_min_f32_e32 v144, 0x40e00000, v190
	v_min_f32_e32 v145, 0x40e00000, v191
	v_mul_f32_e32 v190, s50, v144
	v_mul_f32_e32 v191, s50, v145
	v_med3_f32 v194, v198, s9, v183
	v_exp_f32_e32 v190, v190
	v_exp_f32_e32 v191, v191
	v_med3_f32 v195, v199, s9, v183
	v_mul_f32_e32 v144, v144, v194
	v_mul_f32_e32 v145, v145, v195
	v_add_f32_e32 v200, 1.0, v200
	v_add_f32_e32 v201, 1.0, v201
	v_add_f32_e32 v190, 1.0, v190
	v_add_f32_e32 v191, 1.0, v191
	v_rcp_f32_e32 v200, v200
	v_rcp_f32_e32 v190, v190
	v_rcp_f32_e32 v191, v191
	v_rcp_f32_e32 v201, v201
	v_med3_f32 v194, v196, s9, v183
	v_med3_f32 v195, v197, s9, v183
	v_mul_f32_e32 v190, v144, v190
	v_mul_f32_e32 v191, v145, v191
	v_min_f32_e32 v144, 0x40e00000, v188
	v_min_f32_e32 v145, 0x40e00000, v189
	v_mul_f32_e32 v188, s50, v144
	v_mul_f32_e32 v189, s50, v145
	v_mul_f32_e32 v144, v144, v194
	v_mul_f32_e32 v145, v145, v195
	v_exp_f32_e32 v188, v188
	v_exp_f32_e32 v189, v189
	v_mul_f32_e32 v186, v186, v200
	v_mul_f32_e32 v187, v187, v201
	v_lshlrev_b32_e32 v5, 4, v5
	v_add_u32_e32 v151, v5, v2
	v_add_f32_e32 v188, 1.0, v188
	v_add_f32_e32 v189, 1.0, v189
	v_cmp_gt_i32_e32 vcc, s68, v151
	v_rcp_f32_e32 v188, v188
	v_rcp_f32_e32 v189, v189
	s_nop 0
	v_mul_f32_e32 v188, v144, v188
	v_mul_f32_e32 v189, v145, v189
	v_mov_b32_e32 v144, v3
	v_mov_b32_e32 v145, v3
	v_cvt_pk_fp8_f32 v144, v186, v187
	v_cvt_pk_fp8_f32 v145, v190, v191
	v_cvt_pk_fp8_f32 v144, v192, v193 op_sel:[0,0,1]
	v_cvt_pk_fp8_f32 v145, v188, v189 op_sel:[0,0,1]
	s_nop 0
	v_permlane16_swap_b32_e32 v142, v144
	v_permlane16_swap_b32_e32 v143, v145
	s_and_saveexec_b64 s[0:1], vcc
	s_cbranch_execz .LBB0_1222
	v_add_u32_e32 v186, s69, v151
	v_ashrrev_i32_e32 v187, 31, v186
	v_lshlrev_b64 v[186:187], 10, v[186:187]
	v_lshl_add_u64 v[186:187], s[10:11], 0, v[186:187]
	v_lshl_add_u64 v[186:187], v[186:187], 0, v[164:165]
	v_lshl_add_u64 v[186:187], v[186:187], 0, v[166:167]
	global_store_dwordx4 v[186:187], v[142:145], off
.LBB0_1222:
	s_or_b64 exec, exec, s[0:1]
	s_nop 0
	v_add_f32_e32 v142, v116, v140
	v_add_f32_e32 v143, v117, v141
	v_add_f32_e32 v144, v114, v138
	v_add_f32_e32 v145, v115, v139
	v_add_f32_e32 v192, v82, v170
	v_add_f32_e32 v193, v83, v171
	v_min_f32_e32 v144, 0x40e00000, v144
	v_min_f32_e32 v145, 0x40e00000, v145
	v_med3_f32 v192, v192, s9, v183
	v_med3_f32 v193, v193, s9, v183
	v_min_f32_e32 v142, 0x40e00000, v142
	v_min_f32_e32 v143, 0x40e00000, v143
	v_mul_f32_e32 v198, s50, v144
	v_mul_f32_e32 v199, s50, v145
	v_mul_f32_e32 v144, v144, v192
	v_mul_f32_e32 v145, v145, v193
	v_mul_f32_e32 v192, s50, v142
	v_mul_f32_e32 v193, s50, v143
	v_add_f32_e32 v190, v84, v168
	v_add_f32_e32 v191, v85, v169
	v_exp_f32_e32 v192, v192
	v_exp_f32_e32 v193, v193
	v_med3_f32 v190, v190, s9, v183
	v_med3_f32 v191, v191, s9, v183
	v_add_f32_e32 v188, v110, v134
	v_add_f32_e32 v189, v111, v135
	v_add_f32_e32 v192, 1.0, v192
	v_add_f32_e32 v193, 1.0, v193
	v_mul_f32_e32 v142, v142, v190
	v_mul_f32_e32 v143, v143, v191
	v_rcp_f32_e32 v192, v192
	v_rcp_f32_e32 v193, v193
	v_add_f32_e32 v196, v78, v174
	v_add_f32_e32 v197, v79, v175
	v_add_f32_e32 v186, v112, v136
	v_add_f32_e32 v187, v113, v137
	v_exp_f32_e32 v198, v198
	v_mul_f32_e32 v190, v142, v192
	v_mul_f32_e32 v191, v143, v193
	v_min_f32_e32 v142, 0x40e00000, v188
	v_min_f32_e32 v143, 0x40e00000, v189
	v_mul_f32_e32 v188, s50, v142
	v_mul_f32_e32 v189, s50, v143
	v_med3_f32 v192, v196, s9, v183
	v_exp_f32_e32 v188, v188
	v_exp_f32_e32 v189, v189
	v_med3_f32 v193, v197, s9, v183
	v_mul_f32_e32 v142, v142, v192
	v_mul_f32_e32 v143, v143, v193
	v_exp_f32_e32 v199, v199
	v_add_f32_e32 v188, 1.0, v188
	v_add_f32_e32 v189, 1.0, v189
	v_add_f32_e32 v194, v80, v172
	v_add_f32_e32 v195, v81, v173
	v_rcp_f32_e32 v188, v188
	v_rcp_f32_e32 v189, v189
	v_med3_f32 v192, v194, s9, v183
	v_med3_f32 v193, v195, s9, v183
	v_add_f32_e32 v198, 1.0, v198
	v_add_f32_e32 v199, 1.0, v199
	v_mul_f32_e32 v188, v142, v188
	v_mul_f32_e32 v189, v143, v189
	v_min_f32_e32 v142, 0x40e00000, v186
	v_min_f32_e32 v143, 0x40e00000, v187
	v_mul_f32_e32 v186, s50, v142
	v_mul_f32_e32 v187, s50, v143
	v_mul_f32_e32 v142, v142, v192
	v_mul_f32_e32 v143, v143, v193
	v_exp_f32_e32 v186, v186
	v_exp_f32_e32 v187, v187
	v_rcp_f32_e32 v198, v198
	v_rcp_f32_e32 v199, v199
	v_add_f32_e32 v194, v74, v170
	v_add_f32_e32 v195, v75, v171
	v_add_f32_e32 v186, 1.0, v186
	v_add_f32_e32 v187, 1.0, v187
	v_med3_f32 v194, v194, s9, v183
	v_rcp_f32_e32 v186, v186
	v_rcp_f32_e32 v187, v187
	v_mul_f32_e32 v144, v144, v198
	v_mul_f32_e32 v145, v145, v199
	v_med3_f32 v195, v195, s9, v183
	v_add_f32_e32 v192, v76, v168
	v_add_f32_e32 v193, v77, v169
	v_mul_f32_e32 v186, v142, v186
	v_mul_f32_e32 v187, v143, v187
	v_mov_b32_e32 v143, v3
	v_cvt_pk_fp8_f32 v143, v188, v189
	v_mov_b32_e32 v142, v3
	v_cvt_pk_fp8_f32 v142, v144, v145
	v_add_f32_e32 v144, v108, v140
	v_add_f32_e32 v145, v109, v141
	v_cvt_pk_fp8_f32 v143, v186, v187 op_sel:[0,0,1]
	v_add_f32_e32 v186, v106, v138
	v_add_f32_e32 v187, v107, v139
	v_min_f32_e32 v144, 0x40e00000, v144
	v_min_f32_e32 v186, 0x40e00000, v186
	v_min_f32_e32 v187, 0x40e00000, v187
	v_min_f32_e32 v145, 0x40e00000, v145
	v_mul_f32_e32 v200, s50, v186
	v_mul_f32_e32 v201, s50, v187
	v_mul_f32_e32 v186, v186, v194
	v_mul_f32_e32 v187, v187, v195
	v_mul_f32_e32 v194, s50, v144
	v_mul_f32_e32 v195, s50, v145
	v_med3_f32 v192, v192, s9, v183
	v_exp_f32_e32 v194, v194
	v_exp_f32_e32 v195, v195
	v_med3_f32 v193, v193, s9, v183
	v_cvt_pk_fp8_f32 v142, v190, v191 op_sel:[0,0,1]
	v_add_f32_e32 v190, v102, v134
	v_add_f32_e32 v191, v103, v135
	v_add_f32_e32 v194, 1.0, v194
	v_add_f32_e32 v195, 1.0, v195
	v_mul_f32_e32 v144, v144, v192
	v_mul_f32_e32 v145, v145, v193
	v_rcp_f32_e32 v194, v194
	v_rcp_f32_e32 v195, v195
	v_add_f32_e32 v198, v70, v174
	v_add_f32_e32 v199, v71, v175
	v_add_f32_e32 v188, v104, v136
	v_add_f32_e32 v189, v105, v137
	v_exp_f32_e32 v200, v200
	v_mul_f32_e32 v192, v144, v194
	v_mul_f32_e32 v193, v145, v195
	v_min_f32_e32 v144, 0x40e00000, v190
	v_min_f32_e32 v145, 0x40e00000, v191
	v_mul_f32_e32 v190, s50, v144
	v_mul_f32_e32 v191, s50, v145
	v_med3_f32 v194, v198, s9, v183
	v_exp_f32_e32 v190, v190
	v_exp_f32_e32 v191, v191
	v_med3_f32 v195, v199, s9, v183
	v_mul_f32_e32 v144, v144, v194
	v_mul_f32_e32 v145, v145, v195
	v_exp_f32_e32 v201, v201
	v_add_f32_e32 v190, 1.0, v190
	v_add_f32_e32 v191, 1.0, v191
	v_add_f32_e32 v196, v72, v172
	v_add_f32_e32 v197, v73, v173
	v_rcp_f32_e32 v190, v190
	v_rcp_f32_e32 v191, v191
	v_add_f32_e32 v200, 1.0, v200
	v_add_f32_e32 v201, 1.0, v201
	v_med3_f32 v194, v196, s9, v183
	v_rcp_f32_e32 v200, v200
	v_mul_f32_e32 v190, v144, v190
	v_mul_f32_e32 v191, v145, v191
	v_min_f32_e32 v144, 0x40e00000, v188
	v_min_f32_e32 v145, 0x40e00000, v189
	v_mul_f32_e32 v188, s50, v144
	v_mul_f32_e32 v189, s50, v145
	v_rcp_f32_e32 v201, v201
	v_exp_f32_e32 v188, v188
	v_exp_f32_e32 v189, v189
	v_med3_f32 v195, v197, s9, v183
	v_mul_f32_e32 v144, v144, v194
	v_mul_f32_e32 v145, v145, v195
	v_mul_f32_e32 v186, v186, v200
	v_mul_f32_e32 v187, v187, v201
	v_add_f32_e32 v188, 1.0, v188
	v_add_f32_e32 v189, 1.0, v189
	v_add_u32_e32 v151, 32, v5
	v_rcp_f32_e32 v188, v188
	v_rcp_f32_e32 v189, v189
	v_add_u32_e32 v163, v151, v2
	v_cmp_gt_i32_e32 vcc, s68, v163
	v_mul_f32_e32 v188, v144, v188
	v_mul_f32_e32 v189, v145, v189
	v_mov_b32_e32 v144, v3
	v_mov_b32_e32 v145, v3
	v_cvt_pk_fp8_f32 v144, v186, v187
	v_cvt_pk_fp8_f32 v145, v190, v191
	v_cvt_pk_fp8_f32 v144, v192, v193 op_sel:[0,0,1]
	v_cvt_pk_fp8_f32 v145, v188, v189 op_sel:[0,0,1]
	s_nop 0
	v_permlane16_swap_b32_e32 v142, v144
	v_permlane16_swap_b32_e32 v143, v145
	s_and_saveexec_b64 s[0:1], vcc
	s_cbranch_execz .LBB0_1224
	v_add_u32_e32 v186, s69, v163
	v_ashrrev_i32_e32 v187, 31, v186
	v_lshlrev_b64 v[186:187], 10, v[186:187]
	v_lshl_add_u64 v[186:187], s[10:11], 0, v[186:187]
	v_lshl_add_u64 v[186:187], v[186:187], 0, v[164:165]
	v_lshl_add_u64 v[186:187], v[186:187], 0, v[166:167]
	global_store_dwordx4 v[186:187], v[142:145], off
.LBB0_1224:
	s_or_b64 exec, exec, s[0:1]
	s_nop 0
	v_add_f32_e32 v142, v68, v140
	v_add_f32_e32 v143, v69, v141
	v_add_f32_e32 v144, v66, v138
	v_add_f32_e32 v145, v67, v139
	v_add_f32_e32 v192, v34, v170
	v_add_f32_e32 v193, v35, v171
	v_min_f32_e32 v144, 0x40e00000, v144
	v_min_f32_e32 v145, 0x40e00000, v145
	v_med3_f32 v192, v192, s9, v183
	v_med3_f32 v193, v193, s9, v183
	v_min_f32_e32 v142, 0x40e00000, v142
	v_min_f32_e32 v143, 0x40e00000, v143
	v_mul_f32_e32 v198, s50, v144
	v_mul_f32_e32 v199, s50, v145
	v_mul_f32_e32 v144, v144, v192
	v_mul_f32_e32 v145, v145, v193
	v_mul_f32_e32 v192, s50, v142
	v_mul_f32_e32 v193, s50, v143
	v_add_f32_e32 v190, v36, v168
	v_add_f32_e32 v191, v37, v169
	v_exp_f32_e32 v192, v192
	v_exp_f32_e32 v193, v193
	v_med3_f32 v190, v190, s9, v183
	v_med3_f32 v191, v191, s9, v183
	v_add_f32_e32 v188, v62, v134
	v_add_f32_e32 v189, v63, v135
	v_add_f32_e32 v192, 1.0, v192
	v_add_f32_e32 v193, 1.0, v193
	v_mul_f32_e32 v142, v142, v190
	v_mul_f32_e32 v143, v143, v191
	v_rcp_f32_e32 v192, v192
	v_rcp_f32_e32 v193, v193
	v_add_f32_e32 v196, v30, v174
	v_add_f32_e32 v197, v31, v175
	v_add_f32_e32 v186, v64, v136
	v_add_f32_e32 v187, v65, v137
	v_exp_f32_e32 v198, v198
	v_mul_f32_e32 v190, v142, v192
	v_mul_f32_e32 v191, v143, v193
	v_min_f32_e32 v142, 0x40e00000, v188
	v_min_f32_e32 v143, 0x40e00000, v189
	v_mul_f32_e32 v188, s50, v142
	v_mul_f32_e32 v189, s50, v143
	v_med3_f32 v192, v196, s9, v183
	v_exp_f32_e32 v188, v188
	v_exp_f32_e32 v189, v189
	v_med3_f32 v193, v197, s9, v183
	v_mul_f32_e32 v142, v142, v192
	v_mul_f32_e32 v143, v143, v193
	v_exp_f32_e32 v199, v199
	v_add_f32_e32 v188, 1.0, v188
	v_add_f32_e32 v189, 1.0, v189
	v_add_f32_e32 v194, v32, v172
	v_add_f32_e32 v195, v33, v173
	v_rcp_f32_e32 v188, v188
	v_rcp_f32_e32 v189, v189
	v_med3_f32 v192, v194, s9, v183
	v_med3_f32 v193, v195, s9, v183
	v_add_f32_e32 v198, 1.0, v198
	v_add_f32_e32 v199, 1.0, v199
	v_mul_f32_e32 v188, v142, v188
	v_mul_f32_e32 v189, v143, v189
	v_min_f32_e32 v142, 0x40e00000, v186
	v_min_f32_e32 v143, 0x40e00000, v187
	v_mul_f32_e32 v186, s50, v142
	v_mul_f32_e32 v187, s50, v143
	v_mul_f32_e32 v142, v142, v192
	v_mul_f32_e32 v143, v143, v193
	v_exp_f32_e32 v186, v186
	v_exp_f32_e32 v187, v187
	v_rcp_f32_e32 v198, v198
	v_rcp_f32_e32 v199, v199
	v_add_f32_e32 v194, v26, v170
	v_add_f32_e32 v195, v27, v171
	v_add_f32_e32 v186, 1.0, v186
	v_add_f32_e32 v187, 1.0, v187
	v_med3_f32 v194, v194, s9, v183
	v_rcp_f32_e32 v186, v186
	v_rcp_f32_e32 v187, v187
	v_mul_f32_e32 v144, v144, v198
	v_mul_f32_e32 v145, v145, v199
	v_med3_f32 v195, v195, s9, v183
	v_add_f32_e32 v192, v28, v168
	v_add_f32_e32 v193, v29, v169
	v_mul_f32_e32 v186, v142, v186
	v_mul_f32_e32 v187, v143, v187
	v_mov_b32_e32 v143, v3
	v_cvt_pk_fp8_f32 v143, v188, v189
	v_mov_b32_e32 v142, v3
	v_cvt_pk_fp8_f32 v142, v144, v145
	v_add_f32_e32 v144, v60, v140
	v_add_f32_e32 v145, v61, v141
	v_cvt_pk_fp8_f32 v143, v186, v187 op_sel:[0,0,1]
	v_add_f32_e32 v186, v58, v138
	v_add_f32_e32 v187, v59, v139
	v_min_f32_e32 v144, 0x40e00000, v144
	v_min_f32_e32 v186, 0x40e00000, v186
	v_min_f32_e32 v187, 0x40e00000, v187
	v_min_f32_e32 v145, 0x40e00000, v145
	v_mul_f32_e32 v200, s50, v186
	v_mul_f32_e32 v201, s50, v187
	v_mul_f32_e32 v186, v186, v194
	v_mul_f32_e32 v187, v187, v195
	v_mul_f32_e32 v194, s50, v144
	v_mul_f32_e32 v195, s50, v145
	v_med3_f32 v192, v192, s9, v183
	v_exp_f32_e32 v194, v194
	v_exp_f32_e32 v195, v195
	v_med3_f32 v193, v193, s9, v183
	v_cvt_pk_fp8_f32 v142, v190, v191 op_sel:[0,0,1]
	v_add_f32_e32 v190, v54, v134
	v_add_f32_e32 v191, v55, v135
	v_add_f32_e32 v194, 1.0, v194
	v_add_f32_e32 v195, 1.0, v195
	v_mul_f32_e32 v144, v144, v192
	v_mul_f32_e32 v145, v145, v193
	v_rcp_f32_e32 v194, v194
	v_rcp_f32_e32 v195, v195
	v_add_f32_e32 v198, v22, v174
	v_add_f32_e32 v199, v23, v175
	v_add_f32_e32 v188, v56, v136
	v_add_f32_e32 v189, v57, v137
	v_exp_f32_e32 v200, v200
	v_mul_f32_e32 v192, v144, v194
	v_mul_f32_e32 v193, v145, v195
	v_min_f32_e32 v144, 0x40e00000, v190
	v_min_f32_e32 v145, 0x40e00000, v191
	v_mul_f32_e32 v190, s50, v144
	v_mul_f32_e32 v191, s50, v145
	v_med3_f32 v194, v198, s9, v183
	v_exp_f32_e32 v190, v190
	v_exp_f32_e32 v191, v191
	v_med3_f32 v195, v199, s9, v183
	v_mul_f32_e32 v144, v144, v194
	v_mul_f32_e32 v145, v145, v195
	v_exp_f32_e32 v201, v201
	v_add_f32_e32 v190, 1.0, v190
	v_add_f32_e32 v191, 1.0, v191
	v_add_f32_e32 v196, v24, v172
	v_add_f32_e32 v197, v25, v173
	v_rcp_f32_e32 v190, v190
	v_rcp_f32_e32 v191, v191
	v_add_f32_e32 v200, 1.0, v200
	v_add_f32_e32 v201, 1.0, v201
	v_med3_f32 v194, v196, s9, v183
	v_rcp_f32_e32 v200, v200
	v_mul_f32_e32 v190, v144, v190
	v_mul_f32_e32 v191, v145, v191
	v_min_f32_e32 v144, 0x40e00000, v188
	v_min_f32_e32 v145, 0x40e00000, v189
	v_mul_f32_e32 v188, s50, v144
	v_mul_f32_e32 v189, s50, v145
	v_rcp_f32_e32 v201, v201
	v_exp_f32_e32 v188, v188
	v_exp_f32_e32 v189, v189
	v_med3_f32 v195, v197, s9, v183
	v_mul_f32_e32 v144, v144, v194
	v_mul_f32_e32 v145, v145, v195
	v_mul_f32_e32 v186, v186, v200
	v_mul_f32_e32 v187, v187, v201
	v_add_f32_e32 v188, 1.0, v188
	v_add_f32_e32 v189, 1.0, v189
	v_add_u32_e32 v2, 0x80, v2
	v_rcp_f32_e32 v188, v188
	v_rcp_f32_e32 v189, v189
	v_add_u32_e32 v5, v5, v2
	v_cmp_gt_i32_e32 vcc, s68, v5
	v_mul_f32_e32 v188, v144, v188
	v_mul_f32_e32 v189, v145, v189
	v_mov_b32_e32 v144, v3
	v_mov_b32_e32 v145, v3
	v_cvt_pk_fp8_f32 v144, v186, v187
	v_cvt_pk_fp8_f32 v145, v190, v191
	v_cvt_pk_fp8_f32 v144, v192, v193 op_sel:[0,0,1]
	v_cvt_pk_fp8_f32 v145, v188, v189 op_sel:[0,0,1]
	s_nop 0
	v_permlane16_swap_b32_e32 v142, v144
	v_permlane16_swap_b32_e32 v143, v145
	s_and_saveexec_b64 s[0:1], vcc
	s_cbranch_execz .LBB0_1226
	v_add_u32_e32 v186, s69, v5
	v_ashrrev_i32_e32 v187, 31, v186
	v_lshlrev_b64 v[186:187], 10, v[186:187]
	v_lshl_add_u64 v[186:187], s[10:11], 0, v[186:187]
	v_lshl_add_u64 v[186:187], v[186:187], 0, v[164:165]
	v_lshl_add_u64 v[186:187], v[186:187], 0, v[166:167]
	global_store_dwordx4 v[186:187], v[142:145], off
.LBB0_1226:
	s_or_b64 exec, exec, s[0:1]
	s_nop 0
	v_add_f32_e32 v142, v52, v140
	v_add_f32_e32 v143, v53, v141
	v_add_f32_e32 v144, v50, v138
	v_add_f32_e32 v145, v51, v139
	v_add_f32_e32 v192, v18, v170
	v_add_f32_e32 v193, v19, v171
	v_min_f32_e32 v144, 0x40e00000, v144
	v_min_f32_e32 v145, 0x40e00000, v145
	v_med3_f32 v192, v192, s9, v183
	v_med3_f32 v193, v193, s9, v183
	v_min_f32_e32 v142, 0x40e00000, v142
	v_min_f32_e32 v143, 0x40e00000, v143
	v_mul_f32_e32 v198, s50, v144
	v_mul_f32_e32 v199, s50, v145
	v_mul_f32_e32 v144, v144, v192
	v_mul_f32_e32 v145, v145, v193
	v_mul_f32_e32 v192, s50, v142
	v_mul_f32_e32 v193, s50, v143
	v_add_f32_e32 v190, v20, v168
	v_add_f32_e32 v191, v21, v169
	v_exp_f32_e32 v192, v192
	v_exp_f32_e32 v193, v193
	v_med3_f32 v190, v190, s9, v183
	v_med3_f32 v191, v191, s9, v183
	v_add_f32_e32 v188, v46, v134
	v_add_f32_e32 v189, v47, v135
	v_add_f32_e32 v192, 1.0, v192
	v_add_f32_e32 v193, 1.0, v193
	v_mul_f32_e32 v142, v142, v190
	v_mul_f32_e32 v143, v143, v191
	v_rcp_f32_e32 v192, v192
	v_rcp_f32_e32 v193, v193
	v_add_f32_e32 v196, v14, v174
	v_add_f32_e32 v197, v15, v175
	v_add_f32_e32 v186, v48, v136
	v_add_f32_e32 v187, v49, v137
	v_exp_f32_e32 v198, v198
	v_mul_f32_e32 v190, v142, v192
	v_mul_f32_e32 v191, v143, v193
	v_min_f32_e32 v142, 0x40e00000, v188
	v_min_f32_e32 v143, 0x40e00000, v189
	v_mul_f32_e32 v188, s50, v142
	v_mul_f32_e32 v189, s50, v143
	v_med3_f32 v192, v196, s9, v183
	v_exp_f32_e32 v188, v188
	v_exp_f32_e32 v189, v189
	v_med3_f32 v193, v197, s9, v183
	v_mul_f32_e32 v142, v142, v192
	v_mul_f32_e32 v143, v143, v193
	v_exp_f32_e32 v199, v199
	v_add_f32_e32 v188, 1.0, v188
	v_add_f32_e32 v189, 1.0, v189
	v_add_f32_e32 v194, v16, v172
	v_add_f32_e32 v195, v17, v173
	v_rcp_f32_e32 v188, v188
	v_rcp_f32_e32 v189, v189
	v_add_f32_e32 v198, 1.0, v198
	v_add_f32_e32 v199, 1.0, v199
	v_med3_f32 v192, v194, s9, v183
	v_rcp_f32_e32 v198, v198
	v_mul_f32_e32 v188, v142, v188
	v_mul_f32_e32 v189, v143, v189
	v_min_f32_e32 v142, 0x40e00000, v186
	v_min_f32_e32 v143, 0x40e00000, v187
	v_mul_f32_e32 v186, s50, v142
	v_mul_f32_e32 v187, s50, v143
	v_rcp_f32_e32 v199, v199
	v_exp_f32_e32 v186, v186
	v_exp_f32_e32 v187, v187
	v_med3_f32 v193, v195, s9, v183
	v_mul_f32_e32 v142, v142, v192
	v_mul_f32_e32 v143, v143, v193
	v_mul_f32_e32 v144, v144, v198
	v_mul_f32_e32 v145, v145, v199
	v_add_f32_e32 v186, 1.0, v186
	v_add_f32_e32 v187, 1.0, v187
	v_add_f32_e32 v140, v44, v140
	v_add_f32_e32 v141, v45, v141
	v_rcp_f32_e32 v186, v186
	v_rcp_f32_e32 v187, v187
	v_add_f32_e32 v138, v42, v138
	v_add_f32_e32 v139, v43, v139
	v_min_f32_e32 v140, 0x40e00000, v140
	v_min_f32_e32 v138, 0x40e00000, v138
	v_mul_f32_e32 v186, v142, v186
	v_mul_f32_e32 v187, v143, v187
	v_mov_b32_e32 v142, v3
	v_cvt_pk_fp8_f32 v142, v144, v145
	v_add_f32_e32 v144, v12, v168
	v_add_f32_e32 v145, v13, v169
	v_add_f32_e32 v168, v10, v170
	v_add_f32_e32 v169, v11, v171
	v_min_f32_e32 v139, 0x40e00000, v139
	v_med3_f32 v168, v168, s9, v183
	v_med3_f32 v169, v169, s9, v183
	v_min_f32_e32 v141, 0x40e00000, v141
	v_add_f32_e32 v134, v38, v134
	v_add_f32_e32 v135, v39, v135
	v_add_f32_e32 v170, v8, v172
	v_add_f32_e32 v171, v9, v173
	v_add_f32_e32 v172, v6, v174
	v_add_f32_e32 v173, v7, v175
	v_mul_f32_e32 v174, s50, v138
	v_mul_f32_e32 v175, s50, v139
	v_mul_f32_e32 v138, v138, v168
	v_mul_f32_e32 v139, v139, v169
	v_mul_f32_e32 v168, s50, v140
	v_mul_f32_e32 v169, s50, v141
	v_med3_f32 v144, v144, s9, v183
	v_exp_f32_e32 v168, v168
	v_exp_f32_e32 v169, v169
	v_med3_f32 v145, v145, s9, v183
	v_min_f32_e32 v134, 0x40e00000, v134
	v_min_f32_e32 v135, 0x40e00000, v135
	v_mul_f32_e32 v140, v140, v144
	v_mul_f32_e32 v141, v141, v145
	v_mul_f32_e32 v144, s50, v134
	v_mul_f32_e32 v145, s50, v135
	v_add_f32_e32 v168, 1.0, v168
	v_add_f32_e32 v169, 1.0, v169
	v_exp_f32_e32 v144, v144
	v_exp_f32_e32 v145, v145
	v_rcp_f32_e32 v168, v168
	v_rcp_f32_e32 v169, v169
	v_add_f32_e32 v136, v40, v136
	v_add_f32_e32 v137, v41, v137
	v_add_f32_e32 v144, 1.0, v144
	v_add_f32_e32 v145, 1.0, v145
	v_min_f32_e32 v136, 0x40e00000, v136
	v_rcp_f32_e32 v144, v144
	v_rcp_f32_e32 v145, v145
	v_mul_f32_e32 v140, v140, v168
	v_mul_f32_e32 v141, v141, v169
	v_med3_f32 v168, v172, s9, v183
	v_med3_f32 v169, v173, s9, v183
	v_mul_f32_e32 v134, v134, v168
	v_mul_f32_e32 v135, v135, v169
	v_min_f32_e32 v137, 0x40e00000, v137
	v_mul_f32_e32 v134, v134, v144
	v_mul_f32_e32 v135, v135, v145
	v_mul_f32_e32 v144, s50, v136
	v_mul_f32_e32 v145, s50, v137
	v_exp_f32_e32 v174, v174
	v_exp_f32_e32 v175, v175
	v_exp_f32_e32 v144, v144
	v_exp_f32_e32 v145, v145
	v_med3_f32 v168, v170, s9, v183
	v_add_f32_e32 v174, 1.0, v174
	v_add_f32_e32 v175, 1.0, v175
	v_med3_f32 v169, v171, s9, v183
	v_add_f32_e32 v144, 1.0, v144
	v_add_f32_e32 v145, 1.0, v145
	v_rcp_f32_e32 v174, v174
	v_rcp_f32_e32 v175, v175
	v_rcp_f32_e32 v144, v144
	v_rcp_f32_e32 v145, v145
	v_mul_f32_e32 v136, v136, v168
	v_mul_f32_e32 v137, v137, v169
	v_mov_b32_e32 v143, v3
	v_mul_f32_e32 v138, v138, v174
	v_mul_f32_e32 v139, v139, v175
	v_mul_f32_e32 v136, v136, v144
	v_mul_f32_e32 v137, v137, v145
	v_mov_b32_e32 v144, v3
	v_mov_b32_e32 v145, v3
	v_cvt_pk_fp8_f32 v143, v188, v189
	v_cvt_pk_fp8_f32 v144, v138, v139
	v_cvt_pk_fp8_f32 v145, v134, v135
	v_cvt_pk_fp8_f32 v142, v190, v191 op_sel:[0,0,1]
	v_cvt_pk_fp8_f32 v143, v186, v187 op_sel:[0,0,1]
	v_cvt_pk_fp8_f32 v144, v140, v141 op_sel:[0,0,1]
	v_cvt_pk_fp8_f32 v145, v136, v137 op_sel:[0,0,1]
	v_add_u32_e32 v2, v151, v2
	v_cmp_gt_i32_e32 vcc, s68, v2
	v_permlane16_swap_b32_e32 v142, v144
	v_permlane16_swap_b32_e32 v143, v145
	s_and_saveexec_b64 s[0:1], vcc
	s_cbranch_execnz .LBB0_1228
	s_or_b64 exec, exec, s[0:1]
	s_andn2_b64 vcc, exec, s[74:75]
	s_cbranch_vccnz .LBB0_1197
	s_branch .LBB0_1229

.LBB0_1321:
	s_lshl_b32 s2, s82, 10
	s_nop 15
	s_nop 15
	s_and_b32 s2, s2, 0x400
	v_add_u32_e32 v0, s2, v173
	v_mov_b32_e32 v148, v168
	ds_read_b128 v[144:147], v0
	ds_read_b128 v[140:143], v0 offset:16
	ds_read_b128 v[4:7], v0 offset:512
	ds_read_b128 v[0:3], v0 offset:528
	s_and_b32 s3, s81, 0x300
	v_lshlrev_b32_e32 v155, 4, v148
	v_add_u32_e32 v177, v155, v169
	v_lshlrev_b32_e32 v10, 3, v148
	v_add_u32_e32 v148, s62, v177
	v_ashrrev_i32_e32 v149, 31, v148
	v_lshlrev_b64 v[148:149], 10, v[148:149]
	v_or_b32_e32 v8, s3, v171
	v_ashrrev_i32_e32 v11, 31, v10
	v_sub_co_u32_e32 v10, vcc, 0, v10
	v_lshl_add_u64 v[148:149], s[12:13], 0, v[148:149]
	s_nop 0
	v_subb_co_u32_e32 v11, vcc, 0, v11, vcc
	v_lshl_add_u64 v[148:149], v[148:149], 0, v[8:9]
	v_lshl_add_u64 v[166:167], v[148:149], 0, v[10:11]
	s_waitcnt lgkmcnt(0)
	v_add_f32_e32 v150, v120, v144
	v_add_f32_e32 v151, v121, v145
	v_add_f32_e32 v178, v116, v140
	v_add_f32_e32 v179, v117, v141
	v_mov_b32_e32 v148, v9
	v_mov_b32_e32 v149, v9
	v_cvt_pk_fp8_f32 v148, v150, v151
	v_cvt_pk_fp8_f32 v149, v178, v179
	v_add_f32_e32 v150, v122, v146
	v_add_f32_e32 v151, v123, v147
	v_add_f32_e32 v178, v118, v142
	v_add_f32_e32 v179, v119, v143
	v_cvt_pk_fp8_f32 v148, v150, v151 op_sel:[0,0,1]
	v_cvt_pk_fp8_f32 v149, v178, v179 op_sel:[0,0,1]
	v_add_f32_e32 v178, v112, v144
	v_add_f32_e32 v179, v113, v145
	v_mov_b32_e32 v150, v9
	v_add_f32_e32 v180, v108, v140
	v_add_f32_e32 v181, v109, v141
	v_cvt_pk_fp8_f32 v150, v178, v179
	v_mov_b32_e32 v151, v9
	v_cvt_pk_fp8_f32 v151, v180, v181
	v_add_f32_e32 v178, v114, v146
	v_add_f32_e32 v179, v115, v147
	v_cmp_gt_i32_e32 vcc, s35, v177
	v_cvt_pk_fp8_f32 v150, v178, v179 op_sel:[0,0,1]
	v_add_f32_e32 v178, v110, v142
	v_add_f32_e32 v179, v111, v143
	s_nop 0
	v_permlane16_swap_b32_e32 v148, v150
	v_cvt_pk_fp8_f32 v151, v178, v179 op_sel:[0,0,1]
	s_nop 1
	v_permlane16_swap_b32_e32 v149, v151
	s_and_saveexec_b64 s[2:3], vcc
	s_cbranch_execz .LBB0_1323
	global_store_dwordx4 v[166:167], v[148:151], off
.LBB0_1323:
	s_or_b64 exec, exec, s[2:3]
	s_nop 0
	v_add_f32_e32 v150, v88, v4
	v_add_f32_e32 v151, v89, v5
	v_add_f32_e32 v178, v84, v0
	v_add_f32_e32 v179, v85, v1
	v_mov_b32_e32 v148, v9
	v_mov_b32_e32 v149, v9
	v_cvt_pk_fp8_f32 v148, v150, v151
	v_cvt_pk_fp8_f32 v149, v178, v179
	v_add_f32_e32 v150, v90, v6
	v_add_f32_e32 v151, v91, v7
	v_add_f32_e32 v178, v86, v2
	v_add_f32_e32 v179, v87, v3
	v_cvt_pk_fp8_f32 v148, v150, v151 op_sel:[0,0,1]
	v_cvt_pk_fp8_f32 v149, v178, v179 op_sel:[0,0,1]
	v_add_f32_e32 v178, v80, v4
	v_add_f32_e32 v179, v81, v5
	v_mov_b32_e32 v150, v9
	v_add_f32_e32 v180, v76, v0
	v_add_f32_e32 v181, v77, v1
	v_cvt_pk_fp8_f32 v150, v178, v179
	v_mov_b32_e32 v151, v9
	v_cvt_pk_fp8_f32 v151, v180, v181
	v_add_f32_e32 v178, v82, v6
	v_add_f32_e32 v179, v83, v7
	s_nop 0
	v_cvt_pk_fp8_f32 v150, v178, v179 op_sel:[0,0,1]
	v_add_f32_e32 v178, v78, v2
	v_add_f32_e32 v179, v79, v3
	s_nop 0
	v_permlane16_swap_b32_e32 v148, v150
	v_cvt_pk_fp8_f32 v151, v178, v179 op_sel:[0,0,1]
	s_nop 1
	v_permlane16_swap_b32_e32 v149, v151
	s_and_saveexec_b64 s[2:3], vcc
	s_cbranch_execz .LBB0_1325
	global_store_dwordx4 v[166:167], v[148:151], off offset:128
.LBB0_1325:
	s_or_b64 exec, exec, s[2:3]
	v_add_u32_e32 v177, 32, v155
	v_add_u32_e32 v182, v177, v169
	v_add_u32_e32 v148, s62, v182
	v_ashrrev_i32_e32 v149, 31, v148
	v_lshlrev_b64 v[148:149], 10, v[148:149]
	v_lshl_add_u64 v[148:149], s[12:13], 0, v[148:149]
	v_lshl_add_u64 v[148:149], v[148:149], 0, v[8:9]
	v_lshl_add_u64 v[166:167], v[148:149], 0, v[10:11]
	v_add_f32_e32 v150, v104, v144
	v_add_f32_e32 v151, v105, v145
	v_add_f32_e32 v178, v100, v140
	v_add_f32_e32 v179, v101, v141
	v_mov_b32_e32 v148, v9
	v_mov_b32_e32 v149, v9
	v_cvt_pk_fp8_f32 v148, v150, v151
	v_cvt_pk_fp8_f32 v149, v178, v179
	v_add_f32_e32 v150, v106, v146
	v_add_f32_e32 v151, v107, v147
	v_add_f32_e32 v178, v102, v142
	v_add_f32_e32 v179, v103, v143
	v_cvt_pk_fp8_f32 v148, v150, v151 op_sel:[0,0,1]
	v_cvt_pk_fp8_f32 v149, v178, v179 op_sel:[0,0,1]
	v_add_f32_e32 v178, v96, v144
	v_add_f32_e32 v179, v97, v145
	v_mov_b32_e32 v150, v9
	v_add_f32_e32 v180, v92, v140
	v_add_f32_e32 v181, v93, v141
	v_cvt_pk_fp8_f32 v150, v178, v179
	v_mov_b32_e32 v151, v9
	v_cvt_pk_fp8_f32 v151, v180, v181
	v_add_f32_e32 v178, v98, v146
	v_add_f32_e32 v179, v99, v147
	v_cmp_gt_i32_e32 vcc, s35, v182
	v_cvt_pk_fp8_f32 v150, v178, v179 op_sel:[0,0,1]
	v_add_f32_e32 v178, v94, v142
	v_add_f32_e32 v179, v95, v143
	s_nop 0
	v_permlane16_swap_b32_e32 v148, v150
	v_cvt_pk_fp8_f32 v151, v178, v179 op_sel:[0,0,1]
	s_nop 1
	v_permlane16_swap_b32_e32 v149, v151
	s_and_saveexec_b64 s[2:3], vcc
	s_cbranch_execz .LBB0_1327
	global_store_dwordx4 v[166:167], v[148:151], off
.LBB0_1327:
	s_or_b64 exec, exec, s[2:3]
	s_nop 0
	v_add_f32_e32 v150, v72, v4
	v_add_f32_e32 v151, v73, v5
	v_add_f32_e32 v178, v68, v0
	v_add_f32_e32 v179, v69, v1
	v_mov_b32_e32 v148, v9
	v_mov_b32_e32 v149, v9
	v_cvt_pk_fp8_f32 v148, v150, v151
	v_cvt_pk_fp8_f32 v149, v178, v179
	v_add_f32_e32 v150, v74, v6
	v_add_f32_e32 v151, v75, v7
	v_add_f32_e32 v178, v70, v2
	v_add_f32_e32 v179, v71, v3
	v_cvt_pk_fp8_f32 v148, v150, v151 op_sel:[0,0,1]
	v_cvt_pk_fp8_f32 v149, v178, v179 op_sel:[0,0,1]
	v_add_f32_e32 v178, v64, v4
	v_add_f32_e32 v179, v65, v5
	v_mov_b32_e32 v150, v9
	v_add_f32_e32 v180, v60, v0
	v_add_f32_e32 v181, v61, v1
	v_cvt_pk_fp8_f32 v150, v178, v179
	v_mov_b32_e32 v151, v9
	v_cvt_pk_fp8_f32 v151, v180, v181
	v_add_f32_e32 v178, v66, v6
	v_add_f32_e32 v179, v67, v7
	s_nop 0
	v_cvt_pk_fp8_f32 v150, v178, v179 op_sel:[0,0,1]
	v_add_f32_e32 v178, v62, v2
	v_add_f32_e32 v179, v63, v3
	s_nop 0
	v_permlane16_swap_b32_e32 v148, v150
	v_cvt_pk_fp8_f32 v151, v178, v179 op_sel:[0,0,1]
	s_nop 1
	v_permlane16_swap_b32_e32 v149, v151
	s_and_saveexec_b64 s[2:3], vcc
	s_cbranch_execz .LBB0_1329
	global_store_dwordx4 v[166:167], v[148:151], off offset:128
.LBB0_1329:
	s_or_b64 exec, exec, s[2:3]
	v_add_u32_e32 v155, v155, v172
	v_add_u32_e32 v148, s62, v155
	v_ashrrev_i32_e32 v149, 31, v148
	v_lshlrev_b64 v[148:149], 10, v[148:149]
	v_lshl_add_u64 v[148:149], s[12:13], 0, v[148:149]
	v_lshl_add_u64 v[148:149], v[148:149], 0, v[8:9]
	v_lshl_add_u64 v[166:167], v[148:149], 0, v[10:11]
	v_add_f32_e32 v150, v144, v56
	v_add_f32_e32 v151, v145, v57
	v_add_f32_e32 v178, v52, v140
	v_add_f32_e32 v179, v53, v141
	v_mov_b32_e32 v148, v9
	v_mov_b32_e32 v149, v9
	v_cvt_pk_fp8_f32 v148, v150, v151
	v_cvt_pk_fp8_f32 v149, v178, v179
	v_add_f32_e32 v150, v146, v58
	v_add_f32_e32 v151, v147, v59
	v_add_f32_e32 v178, v54, v142
	v_add_f32_e32 v179, v55, v143
	v_cvt_pk_fp8_f32 v148, v150, v151 op_sel:[0,0,1]
	v_cvt_pk_fp8_f32 v149, v178, v179 op_sel:[0,0,1]
	v_add_f32_e32 v178, v144, v48
	v_add_f32_e32 v179, v145, v49
	v_mov_b32_e32 v150, v9
	v_add_f32_e32 v180, v44, v140
	v_add_f32_e32 v181, v45, v141
	v_cvt_pk_fp8_f32 v150, v178, v179
	v_mov_b32_e32 v151, v9
	v_cvt_pk_fp8_f32 v151, v180, v181
	v_add_f32_e32 v178, v146, v50
	v_add_f32_e32 v179, v147, v51
	v_cmp_gt_i32_e32 vcc, s35, v155
	v_cvt_pk_fp8_f32 v150, v178, v179 op_sel:[0,0,1]
	v_add_f32_e32 v178, v46, v142
	v_add_f32_e32 v179, v47, v143
	s_nop 0
	v_permlane16_swap_b32_e32 v148, v150
	v_cvt_pk_fp8_f32 v151, v178, v179 op_sel:[0,0,1]
	s_nop 1
	v_permlane16_swap_b32_e32 v149, v151
	s_and_saveexec_b64 s[2:3], vcc
	s_cbranch_execz .LBB0_1331
	global_store_dwordx4 v[166:167], v[148:151], off
.LBB0_1331:
	s_or_b64 exec, exec, s[2:3]
	s_nop 0
	v_add_f32_e32 v150, v24, v4
	v_add_f32_e32 v151, v25, v5
	v_add_f32_e32 v178, v20, v0
	v_add_f32_e32 v179, v21, v1
	v_mov_b32_e32 v148, v9
	v_mov_b32_e32 v149, v9
	v_cvt_pk_fp8_f32 v148, v150, v151
	v_cvt_pk_fp8_f32 v149, v178, v179
	v_add_f32_e32 v150, v26, v6
	v_add_f32_e32 v151, v27, v7
	v_add_f32_e32 v178, v22, v2
	v_add_f32_e32 v179, v23, v3
	v_cvt_pk_fp8_f32 v148, v150, v151 op_sel:[0,0,1]
	v_cvt_pk_fp8_f32 v149, v178, v179 op_sel:[0,0,1]
	v_add_f32_e32 v178, v16, v4
	v_add_f32_e32 v179, v17, v5
	v_mov_b32_e32 v150, v9
	v_add_f32_e32 v180, v12, v0
	v_add_f32_e32 v181, v13, v1
	v_cvt_pk_fp8_f32 v150, v178, v179
	v_mov_b32_e32 v151, v9
	v_cvt_pk_fp8_f32 v151, v180, v181
	v_add_f32_e32 v178, v18, v6
	v_add_f32_e32 v179, v19, v7
	s_nop 0
	v_cvt_pk_fp8_f32 v150, v178, v179 op_sel:[0,0,1]
	v_add_f32_e32 v178, v14, v2
	v_add_f32_e32 v179, v15, v3
	s_nop 0
	v_permlane16_swap_b32_e32 v148, v150
	v_cvt_pk_fp8_f32 v151, v178, v179 op_sel:[0,0,1]
	s_nop 1
	v_permlane16_swap_b32_e32 v149, v151
	s_and_saveexec_b64 s[2:3], vcc
	s_cbranch_execz .LBB0_1333
	global_store_dwordx4 v[166:167], v[148:151], off offset:128
.LBB0_1333:
	s_or_b64 exec, exec, s[2:3]
	v_add_u32_e32 v155, v177, v172
	v_add_u32_e32 v148, s62, v155
	v_ashrrev_i32_e32 v149, 31, v148
	v_lshlrev_b64 v[148:149], 10, v[148:149]
	v_lshl_add_u64 v[148:149], s[12:13], 0, v[148:149]
	v_lshl_add_u64 v[148:149], v[148:149], 0, v[8:9]
	v_lshl_add_u64 v[10:11], v[148:149], 0, v[10:11]
	v_add_f32_e32 v150, v144, v40
	v_add_f32_e32 v151, v145, v41
	v_mov_b32_e32 v148, v9
	v_cvt_pk_fp8_f32 v148, v150, v151
	v_add_f32_e32 v150, v146, v42
	v_add_f32_e32 v151, v147, v43
	v_add_f32_e32 v144, v144, v32
	v_add_f32_e32 v145, v145, v33
	v_add_f32_e32 v166, v36, v140
	v_add_f32_e32 v167, v37, v141
	v_cvt_pk_fp8_f32 v148, v150, v151 op_sel:[0,0,1]
	v_mov_b32_e32 v150, v9
	v_mov_b32_e32 v149, v9
	v_add_f32_e32 v140, v28, v140
	v_add_f32_e32 v141, v29, v141
	v_cvt_pk_fp8_f32 v150, v144, v145
	v_mov_b32_e32 v151, v9
	v_cvt_pk_fp8_f32 v149, v166, v167
	v_cvt_pk_fp8_f32 v151, v140, v141
	v_add_f32_e32 v140, v146, v34
	v_add_f32_e32 v141, v147, v35
	v_add_f32_e32 v166, v38, v142
	v_add_f32_e32 v167, v39, v143
	v_cvt_pk_fp8_f32 v150, v140, v141 op_sel:[0,0,1]
	v_add_f32_e32 v140, v30, v142
	v_add_f32_e32 v141, v31, v143
	v_cvt_pk_fp8_f32 v149, v166, v167 op_sel:[0,0,1]
	v_cvt_pk_fp8_f32 v151, v140, v141 op_sel:[0,0,1]
	v_permlane16_swap_b32_e32 v148, v150
	v_cmp_gt_i32_e32 vcc, s35, v155
	v_permlane16_swap_b32_e32 v149, v151
	s_and_saveexec_b64 s[2:3], vcc
	s_cbranch_execz .LBB0_1335
	global_store_dwordx4 v[10:11], v[148:151], off
.LBB0_1335:
	s_or_b64 exec, exec, s[2:3]
	v_add_f32_e32 v142, v124, v4
	v_add_f32_e32 v143, v125, v5
	v_mov_b32_e32 v140, v9
	v_cvt_pk_fp8_f32 v140, v142, v143
	v_add_f32_e32 v142, v126, v6
	v_add_f32_e32 v143, v127, v7
	v_add_f32_e32 v4, v132, v4
	v_add_f32_e32 v5, v133, v5
	v_add_f32_e32 v144, v128, v0
	v_add_f32_e32 v145, v129, v1
	v_cvt_pk_fp8_f32 v140, v142, v143 op_sel:[0,0,1]
	v_mov_b32_e32 v142, v9
	v_mov_b32_e32 v141, v9
	v_add_f32_e32 v0, v136, v0
	v_add_f32_e32 v1, v137, v1
	v_cvt_pk_fp8_f32 v142, v4, v5
	v_mov_b32_e32 v143, v9
	v_cvt_pk_fp8_f32 v141, v144, v145
	v_cvt_pk_fp8_f32 v143, v0, v1
	v_add_f32_e32 v0, v134, v6
	v_add_f32_e32 v1, v135, v7
	v_add_f32_e32 v144, v130, v2
	v_add_f32_e32 v145, v131, v3
	v_cvt_pk_fp8_f32 v142, v0, v1 op_sel:[0,0,1]
	v_add_f32_e32 v0, v138, v2
	v_add_f32_e32 v1, v139, v3
	v_cvt_pk_fp8_f32 v141, v144, v145 op_sel:[0,0,1]
	v_cvt_pk_fp8_f32 v143, v0, v1 op_sel:[0,0,1]
	v_permlane16_swap_b32_e32 v140, v142
	s_nop 0
	v_permlane16_swap_b32_e32 v141, v143
	s_and_saveexec_b64 s[2:3], vcc
	s_cbranch_execnz .LBB0_1337
	s_or_b64 exec, exec, s[2:3]
	s_and_b64 vcc, exec, s[4:5]
	s_cbranch_vccnz .LBB0_1301
	s_branch .LBB0_1338
